# back-edge rotation of both attention tile loops: loop-carried SALU and exit test moved ahead of the per-tile barrier (on top of v45)
# baseline (speedup 1.0000x reference)
.Lat1_body:
	global_load_dwordx4 v[126:129], v[6:7], off
	s_and_saveexec_b64 s[38:39], s[0:1]
	s_cbranch_execz .LBB0_711
	global_load_dwordx4 v[122:125], v[4:5], off

.LBB0_726:
	s_add_i32 s71, s71, 1
	s_mov_b64 s[18:19], 0x80
	v_lshl_add_u64 v[4:5], v[4:5], 0, v[138:139]
	v_lshl_add_u64 v[6:7], v[6:7], 0, v[136:137]
	s_cmp_eq_u32 s67, s75
	v_lshl_add_u64 v[8:9], v[8:9], 0, s[18:19]
	s_cbranch_scc1 .Lat1_exit
	s_mov_b32 s12, s75
	s_mov_b32 s75, s74
	s_mov_b32 s74, s76
	s_cmp_lt_u32 s71, s73
	s_cselect_b64 s[62:63], -1, 0
	s_waitcnt lgkmcnt(0)
	s_barrier
	s_cbranch_scc0 .LBB0_713
	s_branch .Lat1_body
.Lat1_exit:
	s_waitcnt lgkmcnt(0)
	s_barrier
.LBB0_728:
	s_and_b64 vcc, exec, s[64:65]
	s_cbranch_vccz .LBB0_730
	s_mul_i32 s0, s74, 0x2200
	s_add_i32 s0, s0, 0
	v_add3_u32 v3, s0, v3, v159
	v_add_u32_e32 v16, 0x6800, v3
	v_add_u32_e32 v3, 0x7800, v3
	ds_read2_b64 v[4:7], v16 offset1:2
	ds_read2_b64 v[8:11], v16 offset0:4 offset1:6
	ds_read2_b64 v[12:15], v3 offset0:32 offset1:34
	ds_read2_b64 v[50:53], v3 offset0:36 offset1:38
	ds_read2_b64 v[54:57], v16 offset0:8 offset1:10
	ds_read2_b64 v[58:61], v3 offset0:40 offset1:42
	ds_read2_b64 v[62:65], v16 offset0:12 offset1:14
	ds_read2_b64 v[82:85], v3 offset0:44 offset1:46
	s_waitcnt lgkmcnt(7)
	v_mfma_f32_32x32x16_bf16 v[34:49], v[4:7], v[78:81], v[34:49]
	s_waitcnt lgkmcnt(5)
	v_mfma_f32_32x32x16_bf16 v[18:33], v[12:15], v[78:81], v[18:33]
	v_mfma_f32_32x32x16_bf16 v[34:49], v[8:11], v[74:77], v[34:49]
	s_waitcnt lgkmcnt(4)
	v_mfma_f32_32x32x16_bf16 v[18:33], v[50:53], v[74:77], v[18:33]
	s_waitcnt lgkmcnt(3)
	v_mfma_f32_32x32x16_bf16 v[34:49], v[54:57], v[70:73], v[34:49]
	s_waitcnt lgkmcnt(2)
	v_mfma_f32_32x32x16_bf16 v[18:33], v[58:61], v[70:73], v[18:33]
	s_waitcnt lgkmcnt(1)
	v_mfma_f32_32x32x16_bf16 v[34:49], v[62:65], v[66:69], v[34:49]
	s_waitcnt lgkmcnt(0)
	v_mfma_f32_32x32x16_bf16 v[18:33], v[82:85], v[66:69], v[18:33]

.LBB0_774:
	s_add_i32 s55, s55, 1
	s_mov_b64 s[18:19], 0x80
	v_lshl_add_u64 v[4:5], v[4:5], 0, v[138:139]
	v_lshl_add_u64 v[6:7], v[6:7], 0, v[136:137]
	s_cmp_eq_u32 s56, s60
	v_lshl_add_u64 v[8:9], v[8:9], 0, s[18:19]
	s_cbranch_scc1 .Lat2_exit
	s_mov_b32 s12, s60
	s_mov_b32 s60, s57
	s_mov_b32 s57, s61
	s_cmp_lt_u32 s55, s59
	s_cselect_b64 s[50:51], -1, 0
	s_waitcnt lgkmcnt(0)
	s_barrier
	s_cbranch_scc0 .LBB0_761
	s_branch .Lat2_body
.Lat2_exit:
	s_waitcnt lgkmcnt(0)
	s_barrier
.LBB0_776:
	s_and_b64 vcc, exec, s[52:53]
	s_cbranch_vccz .LBB0_778
	s_mul_i32 s0, s57, 0x2200
	s_add_i32 s0, s0, 0
	v_add3_u32 v3, s0, v3, v159
	v_add_u32_e32 v16, 0x6800, v3
	v_add_u32_e32 v3, 0x7800, v3
	ds_read2_b64 v[4:7], v16 offset1:2
	ds_read2_b64 v[8:11], v16 offset0:4 offset1:6
	ds_read2_b64 v[12:15], v3 offset0:32 offset1:34
	ds_read2_b64 v[50:53], v3 offset0:36 offset1:38
	ds_read2_b64 v[54:57], v16 offset0:8 offset1:10
	ds_read2_b64 v[58:61], v3 offset0:40 offset1:42
	ds_read2_b64 v[62:65], v16 offset0:12 offset1:14
	ds_read2_b64 v[82:85], v3 offset0:44 offset1:46
	s_waitcnt lgkmcnt(7)
	v_mfma_f32_32x32x16_bf16 v[34:49], v[4:7], v[66:69], v[34:49]
	s_waitcnt lgkmcnt(5)
	v_mfma_f32_32x32x16_bf16 v[18:33], v[12:15], v[66:69], v[18:33]
	v_mfma_f32_32x32x16_bf16 v[34:49], v[8:11], v[70:73], v[34:49]
	s_waitcnt lgkmcnt(4)
	v_mfma_f32_32x32x16_bf16 v[18:33], v[50:53], v[70:73], v[18:33]
	s_waitcnt lgkmcnt(3)
	v_mfma_f32_32x32x16_bf16 v[34:49], v[54:57], v[74:77], v[34:49]
	s_waitcnt lgkmcnt(2)
	v_mfma_f32_32x32x16_bf16 v[18:33], v[58:61], v[74:77], v[18:33]
	s_waitcnt lgkmcnt(1)
	v_mfma_f32_32x32x16_bf16 v[34:49], v[62:65], v[78:81], v[34:49]
	s_waitcnt lgkmcnt(0)
	v_mfma_f32_32x32x16_bf16 v[18:33], v[82:85], v[78:81], v[18:33]
